# speedup vs baseline: 1.0074x; 1.0074x over previous
.LBB1_20:
	v_exp_f32_e32 v16, v16
	s_lshl_b32 s15, s13, 4
	v_exp_f32_e32 v17, v17
	s_add_i32 s15, s10, s15
	v_exp_f32_e32 v18, v18
	v_mov_b32_e32 v91, s15
	v_mov_b32_e32 v92, s14
	v_exp_f32_e32 v19, v19
	ds_write_b32 v91, v92
	v_exp_f32_e32 v20, v20
	v_exp_f32_e32 v21, v21
	v_exp_f32_e32 v22, v22
	v_exp_f32_e32 v23, v23
	v_exp_f32_e32 v24, v24
	v_exp_f32_e32 v25, v25
	v_exp_f32_e32 v26, v26
	v_exp_f32_e32 v27, v27
	v_exp_f32_e32 v28, v28
	v_exp_f32_e32 v29, v29
	v_exp_f32_e32 v30, v30
	v_exp_f32_e32 v31, v31
	v_exp_f32_e32 v32, v32
	v_exp_f32_e32 v33, v33
	v_exp_f32_e32 v34, v34
	v_exp_f32_e32 v35, v35
	v_exp_f32_e32 v36, v36
	v_exp_f32_e32 v37, v37
	v_exp_f32_e32 v38, v38
	v_exp_f32_e32 v39, v39
	v_exp_f32_e32 v40, v40
	v_exp_f32_e32 v41, v41
	v_exp_f32_e32 v42, v42
	v_exp_f32_e32 v43, v43
	v_exp_f32_e32 v44, v44
	v_exp_f32_e32 v45, v45
	v_exp_f32_e32 v46, v46
	v_exp_f32_e32 v47, v47
	v_pk_add_f32 v[92:93], v[16:17], v[18:19]
	v_pk_add_f32 v[94:95], v[20:21], v[22:23]
	v_pk_add_f32 v[92:93], v[92:93], v[24:25]
	v_pk_add_f32 v[94:95], v[94:95], v[26:27]
	v_pk_add_f32 v[92:93], v[92:93], v[28:29]
	v_pk_add_f32 v[94:95], v[94:95], v[30:31]
	v_pk_add_f32 v[92:93], v[92:93], v[32:33]
	v_pk_add_f32 v[94:95], v[94:95], v[34:35]
	v_pk_add_f32 v[92:93], v[92:93], v[36:37]
	v_pk_add_f32 v[94:95], v[94:95], v[38:39]
	v_pk_add_f32 v[92:93], v[92:93], v[40:41]
	v_pk_add_f32 v[94:95], v[94:95], v[42:43]
	v_pk_add_f32 v[92:93], v[92:93], v[44:45]
	v_pk_add_f32 v[94:95], v[94:95], v[46:47]
	v_pk_add_f32 v[92:93], v[92:93], v[94:95]
	v_add_f32_e32 v91, v92, v93
	v_add_f32_e32 v99, v99, v91
	v_lshl_add_u32 v91, s13, 14, v89
	v_cvt_pk_bf16_f32 v16, v16, v17
	v_cvt_pk_bf16_f32 v17, v18, v19
	v_cvt_pk_bf16_f32 v18, v20, v21
	v_cvt_pk_bf16_f32 v19, v22, v23
	ds_write_b128 v91, v[16:19]
	v_cvt_pk_bf16_f32 v16, v24, v25
	v_cvt_pk_bf16_f32 v17, v26, v27
	v_cvt_pk_bf16_f32 v18, v28, v29
	v_cvt_pk_bf16_f32 v19, v30, v31
	ds_write_b128 v91, v[16:19] offset:1024
	v_cvt_pk_bf16_f32 v16, v32, v33
	v_cvt_pk_bf16_f32 v17, v34, v35
	v_cvt_pk_bf16_f32 v18, v36, v37
	v_cvt_pk_bf16_f32 v19, v38, v39
	ds_write_b128 v91, v[16:19] offset:2048
	v_cvt_pk_bf16_f32 v16, v40, v41
	v_cvt_pk_bf16_f32 v17, v42, v43
	v_cvt_pk_bf16_f32 v18, v44, v45
	v_cvt_pk_bf16_f32 v19, v46, v47
	ds_write_b128 v91, v[16:19] offset:3072
	s_add_i32 s13, s5, 0x8000
	s_cmp_lg_u32 s5, 0x10000
	s_cselect_b32 s5, s13, 0
	s_add_i32 s11, s11, 1
	s_cmp_eq_u32 s11, 16
	s_waitcnt lgkmcnt(0)
	s_barrier
	s_cbranch_scc1 .LBB1_23
